# plus: the short-conv rows of the mixer phase are done by the workgroup classes without an FNet unit (they have slack now)
# speedup vs baseline: 1.0067x; 1.0067x over previous
.LBB0_1747:
	s_andn2_b64 vcc, exec, s[0:1]
	v_readlane_b32 s34, v253, 18
	s_mov_b32 s0, s80
	v_readlane_b32 s35, v253, 19
	s_cbranch_vccnz .LBB0_1891
	v_readlane_b32 s34, v252, 7
	s_nop 3
	s_sub_i32 s34, s34, 0x80
	v_readlane_b32 s0, v252, 4
	v_readlane_b32 s1, v252, 5
	s_and_b64 s[0:1], s[0:1], exec
	s_cselect_b32 s34, s86, s34
	s_mov_b64 s[0:1], -1
	s_and_b64 vcc, exec, s[42:43]
	s_cbranch_vccz .LBB0_1820
	s_cmp_lt_i32 s69, 24
	s_cbranch_scc1 .LBB0_1819
	s_and_b32 s0, s65, -8
	v_readlane_b32 s1, v252, 3
	s_add_i32 s2, s1, s0
	s_add_i32 s0, s2, s68
	s_add_i32 s23, s67, s0
	s_cmp_ge_i32 s23, s12
	s_branch .Lmoe_site_E
